# P14 EpiKV8 epilogue: 16 dwordx2 stores per wave/tile paired into 8 dwordx4 via v_permlane16_swap (rows m, m+1), on top of v062
# baseline (speedup 1.0000x reference)
.LBB0_951:
	s_ashr_i32 s31, s30, 31
	s_lshl_b64 s[34:35], s[30:31], 17
	s_add_u32 s34, s3, s34
	s_addc_u32 s35, s17, s35
	ds_read_b128 v[14:17], v158
	ds_read_b128 v[18:21], v158 offset:1024
	ds_read_b128 v[30:33], v158 offset:2048
	ds_read_b128 v[34:37], v158 offset:3072
	s_and_b64 s[36:37], s[4:5], exec
	s_cselect_b32 s41, s35, s43
	s_cselect_b32 s40, s34, s42
	s_ashr_i32 s29, s28, 31
	s_lshl_b64 s[36:37], s[28:29], 17
	s_add_u32 s36, s19, s36
	s_addc_u32 s37, s33, s37
	s_and_b64 s[4:5], s[4:5], exec
	s_cselect_b32 s5, s37, s45
	s_cselect_b32 s4, s36, s44
	s_add_u32 s60, s42, 0x10080
	s_addc_u32 s61, s43, 0
	s_add_i32 s65, s39, 0xc000
	v_lshl_add_u64 v[54:55], s[60:61], 0, v[146:147]
	s_mov_b32 m0, s65
	s_add_i32 s29, s39, 0xe000
	ds_read_b128 v[6:9], v159
	ds_read_b128 v[10:13], v159 offset:1024
	ds_read_b128 v[22:25], v159 offset:2048
	ds_read_b128 v[26:29], v159 offset:3072
	ds_read_b128 v[38:41], v159 offset:4096
	ds_read_b128 v[42:45], v159 offset:5120
	ds_read_b128 v[46:49], v159 offset:6144
	ds_read_b128 v[50:53], v159 offset:7168
	global_load_lds_dwordx4 v[54:55], off
	v_lshl_add_u64 v[54:55], s[60:61], 0, v[150:151]
	s_mov_b32 m0, s29
	s_nop 0
	global_load_lds_dwordx4 v[54:55], off
	s_waitcnt lgkmcnt(8)
	s_barrier
	s_waitcnt lgkmcnt(0)
	s_setprio 1
	v_mov_b64_e32 v[124:125], v[4:5]
	v_mov_b64_e32 v[120:121], v[4:5]
	v_mov_b64_e32 v[108:109], v[4:5]
	v_mov_b64_e32 v[104:105], v[4:5]
	v_mov_b64_e32 v[92:93], v[4:5]
	v_mov_b64_e32 v[88:89], v[4:5]
	v_mov_b64_e32 v[60:61], v[4:5]
	v_mov_b64_e32 v[56:57], v[4:5]
	v_mov_b64_e32 v[122:123], v[2:3]
	v_mov_b64_e32 v[118:119], v[2:3]
	v_mov_b64_e32 v[106:107], v[2:3]
	v_mov_b64_e32 v[102:103], v[2:3]
	v_mov_b64_e32 v[90:91], v[2:3]
	v_mov_b64_e32 v[86:87], v[2:3]
	v_mov_b64_e32 v[58:59], v[2:3]
	v_mov_b64_e32 v[54:55], v[2:3]
	s_waitcnt lgkmcnt(0)
	v_mfma_scale_f32_16x16x128_f8f6f4 v[122:125], v[14:21], v[6:13], v[122:125], v160, v160 op_sel_hi:[0,0,0]
	v_mfma_scale_f32_16x16x128_f8f6f4 v[118:121], v[30:37], v[6:13], v[118:121], v160, v160 op_sel_hi:[0,0,0]
	v_mfma_scale_f32_16x16x128_f8f6f4 v[106:109], v[14:21], v[22:29], v[106:109], v160, v160 op_sel_hi:[0,0,0]
	v_mfma_scale_f32_16x16x128_f8f6f4 v[102:105], v[30:37], v[22:29], v[102:105], v160, v160 op_sel_hi:[0,0,0]
	v_mfma_scale_f32_16x16x128_f8f6f4 v[90:93], v[14:21], v[38:45], v[90:93], v160, v160 op_sel_hi:[0,0,0]
	v_mfma_scale_f32_16x16x128_f8f6f4 v[86:89], v[30:37], v[38:45], v[86:89], v160, v160 op_sel_hi:[0,0,0]
	v_mfma_scale_f32_16x16x128_f8f6f4 v[58:61], v[14:21], v[46:53], v[58:61], v160, v160 op_sel_hi:[0,0,0]
	v_mfma_scale_f32_16x16x128_f8f6f4 v[54:57], v[30:37], v[46:53], v[54:57], v160, v160 op_sel_hi:[0,0,0]
	s_setprio 0
	s_barrier
	v_lshl_add_u64 v[140:141], s[44:45], 0, v[148:149]
	s_add_i32 s63, s55, s46
	v_lshl_add_u64 v[62:63], v[140:141], 0, s[6:7]
	s_mov_b32 m0, s63
	v_lshl_add_u64 v[142:143], s[44:45], 0, v[152:153]
	s_add_i32 s31, s63, 0x2000
	ds_read_b128 v[164:167], v161
	ds_read_b128 v[168:171], v161 offset:1024
	ds_read_b128 v[172:175], v161 offset:2048
	ds_read_b128 v[176:179], v161 offset:3072
	global_load_lds_dwordx4 v[62:63], off
	v_lshl_add_u64 v[62:63], v[142:143], 0, s[6:7]
	s_mov_b32 m0, s31
	s_nop 0
	global_load_lds_dwordx4 v[62:63], off
	s_barrier
	s_waitcnt lgkmcnt(0)
	s_setprio 1
	v_mov_b64_e32 v[132:133], v[4:5]
	v_mov_b64_e32 v[128:129], v[4:5]
	v_mov_b64_e32 v[116:117], v[4:5]
	v_mov_b64_e32 v[112:113], v[4:5]
	v_mov_b64_e32 v[100:101], v[4:5]
	v_mov_b64_e32 v[96:97], v[4:5]
	v_mov_b64_e32 v[68:69], v[4:5]
	v_mov_b64_e32 v[64:65], v[4:5]
	v_mov_b64_e32 v[130:131], v[2:3]
	v_mov_b64_e32 v[126:127], v[2:3]
	v_mov_b64_e32 v[114:115], v[2:3]
	v_mov_b64_e32 v[110:111], v[2:3]
	v_mov_b64_e32 v[98:99], v[2:3]
	v_mov_b64_e32 v[94:95], v[2:3]
	v_mov_b64_e32 v[66:67], v[2:3]
	v_mov_b64_e32 v[62:63], v[2:3]
	s_waitcnt lgkmcnt(0)
	v_mfma_scale_f32_16x16x128_f8f6f4 v[130:133], v[164:171], v[6:13], v[130:133], v160, v160 op_sel_hi:[0,0,0]
	v_mfma_scale_f32_16x16x128_f8f6f4 v[126:129], v[172:179], v[6:13], v[126:129], v160, v160 op_sel_hi:[0,0,0]
	v_mfma_scale_f32_16x16x128_f8f6f4 v[114:117], v[164:171], v[22:29], v[114:117], v160, v160 op_sel_hi:[0,0,0]
	v_mfma_scale_f32_16x16x128_f8f6f4 v[110:113], v[172:179], v[22:29], v[110:113], v160, v160 op_sel_hi:[0,0,0]
	v_mfma_scale_f32_16x16x128_f8f6f4 v[98:101], v[164:171], v[38:45], v[98:101], v160, v160 op_sel_hi:[0,0,0]
	v_mfma_scale_f32_16x16x128_f8f6f4 v[94:97], v[172:179], v[38:45], v[94:97], v160, v160 op_sel_hi:[0,0,0]
	v_mfma_scale_f32_16x16x128_f8f6f4 v[66:69], v[164:171], v[46:53], v[66:69], v160, v160 op_sel_hi:[0,0,0]
	v_mfma_scale_f32_16x16x128_f8f6f4 v[62:65], v[172:179], v[46:53], v[62:65], v160, v160 op_sel_hi:[0,0,0]
	s_setprio 0
	v_lshl_add_u64 v[144:145], s[42:43], 0, v[146:147]
	s_mov_b32 m0, s39
	v_lshl_add_u64 v[6:7], v[144:145], 0, s[6:7]
	v_lshl_add_u64 v[154:155], s[42:43], 0, v[150:151]
	s_barrier
	ds_read_b128 v[46:49], v159 offset:16384
	ds_read_b128 v[50:53], v159 offset:17408
	ds_read_b128 v[180:183], v159 offset:18432
	ds_read_b128 v[184:187], v159 offset:19456
	ds_read_b128 v[190:193], v159 offset:20480
	ds_read_b128 v[194:197], v159 offset:21504
	ds_read_b128 v[214:217], v159 offset:22528
	ds_read_b128 v[218:221], v159 offset:23552
	global_load_lds_dwordx4 v[6:7], off
	v_lshl_add_u64 v[6:7], v[154:155], 0, s[6:7]
	s_mov_b32 m0, s48
	s_nop 0
	global_load_lds_dwordx4 v[6:7], off
	s_barrier
	s_waitcnt lgkmcnt(0)
	s_setprio 1
	v_mov_b64_e32 v[76:77], v[4:5]
	v_mov_b64_e32 v[72:73], v[4:5]
	v_mov_b64_e32 v[44:45], v[4:5]
	v_mov_b64_e32 v[40:41], v[4:5]
	v_mov_b64_e32 v[28:29], v[4:5]
	v_mov_b64_e32 v[24:25], v[4:5]
	v_mov_b64_e32 v[12:13], v[4:5]
	v_mov_b64_e32 v[8:9], v[4:5]
	v_mov_b64_e32 v[74:75], v[2:3]
	v_mov_b64_e32 v[70:71], v[2:3]
	v_mov_b64_e32 v[42:43], v[2:3]
	v_mov_b64_e32 v[38:39], v[2:3]
	v_mov_b64_e32 v[26:27], v[2:3]
	v_mov_b64_e32 v[22:23], v[2:3]
	v_mov_b64_e32 v[10:11], v[2:3]
	v_mov_b64_e32 v[6:7], v[2:3]
	s_waitcnt lgkmcnt(0)
	v_mfma_scale_f32_16x16x128_f8f6f4 v[74:77], v[14:21], v[46:53], v[74:77], v160, v160 op_sel_hi:[0,0,0]
	v_mfma_scale_f32_16x16x128_f8f6f4 v[70:73], v[30:37], v[46:53], v[70:73], v160, v160 op_sel_hi:[0,0,0]
	v_mfma_scale_f32_16x16x128_f8f6f4 v[42:45], v[14:21], v[180:187], v[42:45], v160, v160 op_sel_hi:[0,0,0]
	v_mfma_scale_f32_16x16x128_f8f6f4 v[38:41], v[30:37], v[180:187], v[38:41], v160, v160 op_sel_hi:[0,0,0]
	v_mfma_scale_f32_16x16x128_f8f6f4 v[26:29], v[14:21], v[190:197], v[26:29], v160, v160 op_sel_hi:[0,0,0]
	v_mfma_scale_f32_16x16x128_f8f6f4 v[22:25], v[30:37], v[190:197], v[22:25], v160, v160 op_sel_hi:[0,0,0]
	v_mfma_scale_f32_16x16x128_f8f6f4 v[10:13], v[14:21], v[214:221], v[10:13], v160, v160 op_sel_hi:[0,0,0]
	v_mfma_scale_f32_16x16x128_f8f6f4 v[6:9], v[30:37], v[214:221], v[6:9], v160, v160 op_sel_hi:[0,0,0]
	s_setprio 0
	s_barrier
	s_add_u32 s66, s44, 0x10100
	s_addc_u32 s67, s45, 0
	s_add_i32 s61, s56, s46
	v_lshl_add_u64 v[14:15], s[66:67], 0, v[148:149]
	s_mov_b32 m0, s61
	s_add_i32 s60, s61, 0x2000
	global_load_lds_dwordx4 v[14:15], off
	v_lshl_add_u64 v[14:15], s[66:67], 0, v[152:153]
	s_mov_b32 m0, s60
	s_nop 0
	global_load_lds_dwordx4 v[14:15], off
	s_waitcnt vmcnt(6)
	s_barrier
	s_setprio 1
	v_mov_b64_e32 v[84:85], v[4:5]
	v_mov_b64_e32 v[80:81], v[4:5]
	v_mov_b64_e32 v[82:83], v[2:3]
	v_mov_b64_e32 v[78:79], v[2:3]
	v_mfma_scale_f32_16x16x128_f8f6f4 v[82:85], v[164:171], v[46:53], v[82:85], v160, v160 op_sel_hi:[0,0,0]
	v_mfma_scale_f32_16x16x128_f8f6f4 v[78:81], v[172:179], v[46:53], v[78:81], v160, v160 op_sel_hi:[0,0,0]
	v_mov_b64_e32 v[52:53], v[4:5]
	v_mov_b64_e32 v[48:49], v[4:5]
	v_mov_b64_e32 v[36:37], v[4:5]
	v_mov_b64_e32 v[32:33], v[4:5]
	v_mov_b64_e32 v[20:21], v[4:5]
	v_mov_b64_e32 v[16:17], v[4:5]
	v_mov_b64_e32 v[50:51], v[2:3]
	v_mov_b64_e32 v[46:47], v[2:3]
	v_mov_b64_e32 v[34:35], v[2:3]
	v_mov_b64_e32 v[30:31], v[2:3]
	v_mov_b64_e32 v[18:19], v[2:3]
	v_mov_b64_e32 v[14:15], v[2:3]
	v_mfma_scale_f32_16x16x128_f8f6f4 v[50:53], v[164:171], v[180:187], v[50:53], v160, v160 op_sel_hi:[0,0,0]
	v_mfma_scale_f32_16x16x128_f8f6f4 v[46:49], v[172:179], v[180:187], v[46:49], v160, v160 op_sel_hi:[0,0,0]
	v_mfma_scale_f32_16x16x128_f8f6f4 v[34:37], v[164:171], v[190:197], v[34:37], v160, v160 op_sel_hi:[0,0,0]
	v_mfma_scale_f32_16x16x128_f8f6f4 v[30:33], v[172:179], v[190:197], v[30:33], v160, v160 op_sel_hi:[0,0,0]
	v_mfma_scale_f32_16x16x128_f8f6f4 v[18:21], v[164:171], v[214:221], v[18:21], v160, v160 op_sel_hi:[0,0,0]
	v_mfma_scale_f32_16x16x128_f8f6f4 v[14:17], v[172:179], v[214:221], v[14:17], v160, v160 op_sel_hi:[0,0,0]
	s_setprio 0
	s_add_i32 s64, 0, 0x18000
	v_add_u32_e32 v163, s64, v157
	s_barrier
	ds_read_b128 v[166:169], v163
	ds_read_b128 v[170:173], v163 offset:1024
	ds_read_b128 v[174:177], v163 offset:2048
	ds_read_b128 v[178:181], v163 offset:3072
	s_add_u32 s66, s42, 0x10100
	s_addc_u32 s67, s43, 0
	s_mov_b32 m0, s49
	v_lshl_add_u64 v[164:165], s[66:67], 0, v[146:147]
	ds_read_b128 v[190:193], v159 offset:32768
	ds_read_b128 v[194:197], v159 offset:33792
	ds_read_b128 v[214:217], v159 offset:34816
	ds_read_b128 v[218:221], v159 offset:35840
	ds_read_b128 v[222:225], v159 offset:36864
	ds_read_b128 v[226:229], v159 offset:37888
	ds_read_b128 v[230:233], v159 offset:38912
	ds_read_b128 v[234:237], v159 offset:39936
	global_load_lds_dwordx4 v[164:165], off
	v_lshl_add_u64 v[164:165], s[66:67], 0, v[150:151]
	s_mov_b32 m0, s50
	s_nop 0
	global_load_lds_dwordx4 v[164:165], off
	s_waitcnt lgkmcnt(8)
	s_barrier
	s_waitcnt lgkmcnt(0)
	s_setprio 1
	s_waitcnt lgkmcnt(0)
	v_mfma_scale_f32_16x16x128_f8f6f4 v[122:125], v[166:173], v[190:197], v[122:125], v160, v160 op_sel_hi:[0,0,0]
	v_mfma_scale_f32_16x16x128_f8f6f4 v[118:121], v[174:181], v[190:197], v[118:121], v160, v160 op_sel_hi:[0,0,0]
	v_mfma_scale_f32_16x16x128_f8f6f4 v[106:109], v[166:173], v[214:221], v[106:109], v160, v160 op_sel_hi:[0,0,0]
	v_mfma_scale_f32_16x16x128_f8f6f4 v[102:105], v[174:181], v[214:221], v[102:105], v160, v160 op_sel_hi:[0,0,0]
	v_mfma_scale_f32_16x16x128_f8f6f4 v[90:93], v[166:173], v[222:229], v[90:93], v160, v160 op_sel_hi:[0,0,0]
	v_mfma_scale_f32_16x16x128_f8f6f4 v[86:89], v[174:181], v[222:229], v[86:89], v160, v160 op_sel_hi:[0,0,0]
	v_mfma_scale_f32_16x16x128_f8f6f4 v[58:61], v[166:173], v[230:237], v[58:61], v160, v160 op_sel_hi:[0,0,0]
	v_mfma_scale_f32_16x16x128_f8f6f4 v[54:57], v[174:181], v[230:237], v[54:57], v160, v160 op_sel_hi:[0,0,0]
	s_setprio 0
	s_barrier
	s_add_i32 s68, 0, 0x1c000
	s_add_i32 s64, s64, s46
	v_add_u32_e32 v164, s68, v157
	v_lshl_add_u64 v[140:141], v[140:141], 0, s[14:15]
	s_mov_b32 m0, s64
	s_add_i32 s62, s64, 0x2000
	ds_read_b128 v[238:241], v164
	ds_read_b128 v[242:245], v164 offset:1024
	ds_read_b128 v[246:249], v164 offset:2048
	ds_read_b128 v[250:253], v164 offset:3072
	global_load_lds_dwordx4 v[140:141], off
	v_lshl_add_u64 v[140:141], v[142:143], 0, s[14:15]
	s_mov_b32 m0, s62
	s_nop 0
	global_load_lds_dwordx4 v[140:141], off
	s_barrier
	s_waitcnt lgkmcnt(0)
	s_setprio 1
	s_waitcnt lgkmcnt(0)
	v_mfma_scale_f32_16x16x128_f8f6f4 v[130:133], v[238:245], v[190:197], v[130:133], v160, v160 op_sel_hi:[0,0,0]
	v_mfma_scale_f32_16x16x128_f8f6f4 v[126:129], v[246:253], v[190:197], v[126:129], v160, v160 op_sel_hi:[0,0,0]
	v_mfma_scale_f32_16x16x128_f8f6f4 v[114:117], v[238:245], v[214:221], v[114:117], v160, v160 op_sel_hi:[0,0,0]
	v_mfma_scale_f32_16x16x128_f8f6f4 v[110:113], v[246:253], v[214:221], v[110:113], v160, v160 op_sel_hi:[0,0,0]
	v_mfma_scale_f32_16x16x128_f8f6f4 v[98:101], v[238:245], v[222:229], v[98:101], v160, v160 op_sel_hi:[0,0,0]
	v_mfma_scale_f32_16x16x128_f8f6f4 v[94:97], v[246:253], v[222:229], v[94:97], v160, v160 op_sel_hi:[0,0,0]
	v_mfma_scale_f32_16x16x128_f8f6f4 v[66:69], v[238:245], v[230:237], v[66:69], v160, v160 op_sel_hi:[0,0,0]
	v_mfma_scale_f32_16x16x128_f8f6f4 v[62:65], v[246:253], v[230:237], v[62:65], v160, v160 op_sel_hi:[0,0,0]
	s_setprio 0
	s_mov_b32 m0, s51
	v_lshl_add_u64 v[140:141], v[144:145], 0, s[14:15]
	s_barrier
	ds_read_b128 v[190:193], v159 offset:49152
	ds_read_b128 v[194:197], v159 offset:50176
	ds_read_b128 v[214:217], v159 offset:51200
	ds_read_b128 v[218:221], v159 offset:52224
	ds_read_b128 v[222:225], v159 offset:53248
	ds_read_b128 v[226:229], v159 offset:54272
	ds_read_b128 v[230:233], v159 offset:55296
	ds_read_b128 v[234:237], v159 offset:56320
	global_load_lds_dwordx4 v[140:141], off
	v_lshl_add_u64 v[140:141], v[154:155], 0, s[14:15]
	s_mov_b32 m0, s52
	s_nop 0
	global_load_lds_dwordx4 v[140:141], off
	s_barrier
	s_waitcnt lgkmcnt(0)
	s_setprio 1
	s_waitcnt lgkmcnt(0)
	v_mfma_scale_f32_16x16x128_f8f6f4 v[74:77], v[166:173], v[190:197], v[74:77], v160, v160 op_sel_hi:[0,0,0]
	v_mfma_scale_f32_16x16x128_f8f6f4 v[70:73], v[174:181], v[190:197], v[70:73], v160, v160 op_sel_hi:[0,0,0]
	v_mfma_scale_f32_16x16x128_f8f6f4 v[42:45], v[166:173], v[214:221], v[42:45], v160, v160 op_sel_hi:[0,0,0]
	v_mfma_scale_f32_16x16x128_f8f6f4 v[38:41], v[174:181], v[214:221], v[38:41], v160, v160 op_sel_hi:[0,0,0]
	v_mfma_scale_f32_16x16x128_f8f6f4 v[26:29], v[166:173], v[222:229], v[26:29], v160, v160 op_sel_hi:[0,0,0]
	v_mfma_scale_f32_16x16x128_f8f6f4 v[22:25], v[174:181], v[222:229], v[22:25], v160, v160 op_sel_hi:[0,0,0]
	v_mfma_scale_f32_16x16x128_f8f6f4 v[10:13], v[166:173], v[230:237], v[10:13], v160, v160 op_sel_hi:[0,0,0]
	v_mfma_scale_f32_16x16x128_f8f6f4 v[6:9], v[174:181], v[230:237], v[6:9], v160, v160 op_sel_hi:[0,0,0]
	s_setprio 0
	s_barrier
	s_add_u32 s66, s44, 0x10180
	s_addc_u32 s67, s45, 0
	s_add_i32 s45, s68, s46
	v_lshl_add_u64 v[140:141], s[66:67], 0, v[148:149]
	s_mov_b32 m0, s45
	s_add_i32 s44, s45, 0x2000
	global_load_lds_dwordx4 v[140:141], off
	v_lshl_add_u64 v[140:141], s[66:67], 0, v[152:153]
	s_mov_b32 m0, s44
	s_nop 0
	global_load_lds_dwordx4 v[140:141], off
	s_waitcnt vmcnt(6)
	s_barrier
	s_setprio 1
	v_mfma_scale_f32_16x16x128_f8f6f4 v[82:85], v[238:245], v[190:197], v[82:85], v160, v160 op_sel_hi:[0,0,0]
	v_mfma_scale_f32_16x16x128_f8f6f4 v[78:81], v[246:253], v[190:197], v[78:81], v160, v160 op_sel_hi:[0,0,0]
	v_mfma_scale_f32_16x16x128_f8f6f4 v[50:53], v[238:245], v[214:221], v[50:53], v160, v160 op_sel_hi:[0,0,0]
	v_mfma_scale_f32_16x16x128_f8f6f4 v[46:49], v[246:253], v[214:221], v[46:49], v160, v160 op_sel_hi:[0,0,0]
	v_mfma_scale_f32_16x16x128_f8f6f4 v[34:37], v[238:245], v[222:229], v[34:37], v160, v160 op_sel_hi:[0,0,0]
	v_mfma_scale_f32_16x16x128_f8f6f4 v[30:33], v[246:253], v[222:229], v[30:33], v160, v160 op_sel_hi:[0,0,0]
	v_mfma_scale_f32_16x16x128_f8f6f4 v[18:21], v[238:245], v[230:237], v[18:21], v160, v160 op_sel_hi:[0,0,0]
	v_mfma_scale_f32_16x16x128_f8f6f4 v[14:17], v[246:253], v[230:237], v[14:17], v160, v160 op_sel_hi:[0,0,0]
	s_setprio 0
	s_barrier
	ds_read_b128 v[166:169], v158
	ds_read_b128 v[170:173], v158 offset:1024
	ds_read_b128 v[174:177], v158 offset:2048
	ds_read_b128 v[178:181], v158 offset:3072
	s_add_u32 s42, s42, 0x10180
	s_addc_u32 s43, s43, 0
	s_mov_b32 m0, s65
	v_lshl_add_u64 v[140:141], s[42:43], 0, v[146:147]
	ds_read_b128 v[190:193], v159
	ds_read_b128 v[194:197], v159 offset:1024
	ds_read_b128 v[214:217], v159 offset:2048
	ds_read_b128 v[218:221], v159 offset:3072
	ds_read_b128 v[222:225], v159 offset:4096
	ds_read_b128 v[226:229], v159 offset:5120
	ds_read_b128 v[230:233], v159 offset:6144
	ds_read_b128 v[234:237], v159 offset:7168
	global_load_lds_dwordx4 v[140:141], off
	v_lshl_add_u64 v[140:141], s[42:43], 0, v[150:151]
	s_mov_b32 m0, s29
	s_nop 0
	global_load_lds_dwordx4 v[140:141], off
	s_waitcnt lgkmcnt(8)
	s_barrier
	s_waitcnt lgkmcnt(0)
	s_setprio 1
	s_waitcnt lgkmcnt(0)
	v_mfma_scale_f32_16x16x128_f8f6f4 v[122:125], v[166:173], v[190:197], v[122:125], v160, v160 op_sel_hi:[0,0,0]
	v_mfma_scale_f32_16x16x128_f8f6f4 v[118:121], v[174:181], v[190:197], v[118:121], v160, v160 op_sel_hi:[0,0,0]
	v_mfma_scale_f32_16x16x128_f8f6f4 v[106:109], v[166:173], v[214:221], v[106:109], v160, v160 op_sel_hi:[0,0,0]
	v_mfma_scale_f32_16x16x128_f8f6f4 v[102:105], v[174:181], v[214:221], v[102:105], v160, v160 op_sel_hi:[0,0,0]
	v_mfma_scale_f32_16x16x128_f8f6f4 v[90:93], v[166:173], v[222:229], v[90:93], v160, v160 op_sel_hi:[0,0,0]
	v_mfma_scale_f32_16x16x128_f8f6f4 v[86:89], v[174:181], v[222:229], v[86:89], v160, v160 op_sel_hi:[0,0,0]
	v_mfma_scale_f32_16x16x128_f8f6f4 v[58:61], v[166:173], v[230:237], v[58:61], v160, v160 op_sel_hi:[0,0,0]
	v_mfma_scale_f32_16x16x128_f8f6f4 v[54:57], v[174:181], v[230:237], v[54:57], v160, v160 op_sel_hi:[0,0,0]
	s_setprio 0
	s_barrier
	s_mov_b32 m0, s63
	v_lshl_add_u64 v[140:141], s[4:5], 0, v[148:149]
	ds_read_b128 v[238:241], v161
	ds_read_b128 v[242:245], v161 offset:1024
	ds_read_b128 v[246:249], v161 offset:2048
	ds_read_b128 v[250:253], v161 offset:3072
	global_load_lds_dwordx4 v[140:141], off
	v_lshl_add_u64 v[142:143], s[4:5], 0, v[152:153]
	s_mov_b32 m0, s31
	s_nop 0
	global_load_lds_dwordx4 v[142:143], off
	s_barrier
	s_waitcnt lgkmcnt(0)
	s_setprio 1
	s_waitcnt lgkmcnt(0)
	v_mfma_scale_f32_16x16x128_f8f6f4 v[130:133], v[238:245], v[190:197], v[130:133], v160, v160 op_sel_hi:[0,0,0]
	v_mfma_scale_f32_16x16x128_f8f6f4 v[126:129], v[246:253], v[190:197], v[126:129], v160, v160 op_sel_hi:[0,0,0]
	v_mfma_scale_f32_16x16x128_f8f6f4 v[114:117], v[238:245], v[214:221], v[114:117], v160, v160 op_sel_hi:[0,0,0]
	v_mfma_scale_f32_16x16x128_f8f6f4 v[110:113], v[246:253], v[214:221], v[110:113], v160, v160 op_sel_hi:[0,0,0]
	v_mfma_scale_f32_16x16x128_f8f6f4 v[98:101], v[238:245], v[222:229], v[98:101], v160, v160 op_sel_hi:[0,0,0]
	v_mfma_scale_f32_16x16x128_f8f6f4 v[94:97], v[246:253], v[222:229], v[94:97], v160, v160 op_sel_hi:[0,0,0]
	v_mfma_scale_f32_16x16x128_f8f6f4 v[66:69], v[238:245], v[230:237], v[66:69], v160, v160 op_sel_hi:[0,0,0]
	v_mfma_scale_f32_16x16x128_f8f6f4 v[62:65], v[246:253], v[230:237], v[62:65], v160, v160 op_sel_hi:[0,0,0]
	s_setprio 0
	s_mov_b32 m0, s39
	v_lshl_add_u64 v[144:145], s[40:41], 0, v[146:147]
	s_barrier
	ds_read_b128 v[190:193], v159 offset:16384
	ds_read_b128 v[194:197], v159 offset:17408
	ds_read_b128 v[214:217], v159 offset:18432
	ds_read_b128 v[218:221], v159 offset:19456
	ds_read_b128 v[222:225], v159 offset:20480
	ds_read_b128 v[226:229], v159 offset:21504
	ds_read_b128 v[230:233], v159 offset:22528
	ds_read_b128 v[234:237], v159 offset:23552
	global_load_lds_dwordx4 v[144:145], off
	v_lshl_add_u64 v[154:155], s[40:41], 0, v[150:151]
	s_mov_b32 m0, s48
	s_nop 0
	global_load_lds_dwordx4 v[154:155], off
	s_barrier
	s_waitcnt lgkmcnt(0)
	s_setprio 1
	s_waitcnt lgkmcnt(0)
	v_mfma_scale_f32_16x16x128_f8f6f4 v[74:77], v[166:173], v[190:197], v[74:77], v160, v160 op_sel_hi:[0,0,0]
	v_mfma_scale_f32_16x16x128_f8f6f4 v[70:73], v[174:181], v[190:197], v[70:73], v160, v160 op_sel_hi:[0,0,0]
	v_mfma_scale_f32_16x16x128_f8f6f4 v[42:45], v[166:173], v[214:221], v[42:45], v160, v160 op_sel_hi:[0,0,0]
	v_mfma_scale_f32_16x16x128_f8f6f4 v[38:41], v[174:181], v[214:221], v[38:41], v160, v160 op_sel_hi:[0,0,0]
	v_mfma_scale_f32_16x16x128_f8f6f4 v[26:29], v[166:173], v[222:229], v[26:29], v160, v160 op_sel_hi:[0,0,0]
	v_mfma_scale_f32_16x16x128_f8f6f4 v[22:25], v[174:181], v[222:229], v[22:25], v160, v160 op_sel_hi:[0,0,0]
	v_mfma_scale_f32_16x16x128_f8f6f4 v[10:13], v[166:173], v[230:237], v[10:13], v160, v160 op_sel_hi:[0,0,0]
	v_mfma_scale_f32_16x16x128_f8f6f4 v[6:9], v[174:181], v[230:237], v[6:9], v160, v160 op_sel_hi:[0,0,0]
	s_setprio 0
	s_barrier
	s_add_u32 s42, s4, 0x10000
	s_addc_u32 s43, s5, 0
	s_mov_b32 m0, s61
	v_lshl_add_u64 v[166:167], s[42:43], 0, v[148:149]
	global_load_lds_dwordx4 v[166:167], off
	v_lshl_add_u64 v[166:167], s[42:43], 0, v[152:153]
	s_mov_b32 m0, s60
	s_nop 0
	global_load_lds_dwordx4 v[166:167], off
	s_waitcnt vmcnt(6)
	s_barrier
	s_setprio 1
	v_mfma_scale_f32_16x16x128_f8f6f4 v[82:85], v[238:245], v[190:197], v[82:85], v160, v160 op_sel_hi:[0,0,0]
	v_mfma_scale_f32_16x16x128_f8f6f4 v[78:81], v[246:253], v[190:197], v[78:81], v160, v160 op_sel_hi:[0,0,0]
	v_mfma_scale_f32_16x16x128_f8f6f4 v[50:53], v[238:245], v[214:221], v[50:53], v160, v160 op_sel_hi:[0,0,0]
	v_mfma_scale_f32_16x16x128_f8f6f4 v[46:49], v[246:253], v[214:221], v[46:49], v160, v160 op_sel_hi:[0,0,0]
	v_mfma_scale_f32_16x16x128_f8f6f4 v[34:37], v[238:245], v[222:229], v[34:37], v160, v160 op_sel_hi:[0,0,0]
	v_mfma_scale_f32_16x16x128_f8f6f4 v[30:33], v[246:253], v[222:229], v[30:33], v160, v160 op_sel_hi:[0,0,0]
	v_mfma_scale_f32_16x16x128_f8f6f4 v[18:21], v[238:245], v[230:237], v[18:21], v160, v160 op_sel_hi:[0,0,0]
	v_mfma_scale_f32_16x16x128_f8f6f4 v[14:17], v[246:253], v[230:237], v[14:17], v160, v160 op_sel_hi:[0,0,0]
	s_setprio 0
	s_barrier
	ds_read_b128 v[166:169], v163
	ds_read_b128 v[170:173], v163 offset:1024
	ds_read_b128 v[174:177], v163 offset:2048
	ds_read_b128 v[178:181], v163 offset:3072
	s_add_u32 s40, s40, 0x10000
	s_addc_u32 s41, s41, 0
	s_mov_b32 m0, s49
	v_lshl_add_u64 v[182:183], s[40:41], 0, v[146:147]
	ds_read_b128 v[190:193], v159 offset:32768
	ds_read_b128 v[194:197], v159 offset:33792
	ds_read_b128 v[214:217], v159 offset:34816
	ds_read_b128 v[218:221], v159 offset:35840
	ds_read_b128 v[222:225], v159 offset:36864
	ds_read_b128 v[226:229], v159 offset:37888
	ds_read_b128 v[230:233], v159 offset:38912
	ds_read_b128 v[234:237], v159 offset:39936
	global_load_lds_dwordx4 v[182:183], off
	v_lshl_add_u64 v[182:183], s[40:41], 0, v[150:151]
	s_mov_b32 m0, s50
	s_nop 0
	global_load_lds_dwordx4 v[182:183], off
	s_waitcnt lgkmcnt(8)
	s_barrier
	s_waitcnt lgkmcnt(0)
	s_setprio 1
	s_waitcnt lgkmcnt(0)
	v_mfma_scale_f32_16x16x128_f8f6f4 v[122:125], v[166:173], v[190:197], v[122:125], v160, v160 op_sel_hi:[0,0,0]
	v_mfma_scale_f32_16x16x128_f8f6f4 v[118:121], v[174:181], v[190:197], v[118:121], v160, v160 op_sel_hi:[0,0,0]
	v_mfma_scale_f32_16x16x128_f8f6f4 v[106:109], v[166:173], v[214:221], v[106:109], v160, v160 op_sel_hi:[0,0,0]
	v_mfma_scale_f32_16x16x128_f8f6f4 v[102:105], v[174:181], v[214:221], v[102:105], v160, v160 op_sel_hi:[0,0,0]
	v_mfma_scale_f32_16x16x128_f8f6f4 v[90:93], v[166:173], v[222:229], v[90:93], v160, v160 op_sel_hi:[0,0,0]
	v_mfma_scale_f32_16x16x128_f8f6f4 v[86:89], v[174:181], v[222:229], v[86:89], v160, v160 op_sel_hi:[0,0,0]
	v_mfma_scale_f32_16x16x128_f8f6f4 v[58:61], v[166:173], v[230:237], v[58:61], v160, v160 op_sel_hi:[0,0,0]
	v_mfma_scale_f32_16x16x128_f8f6f4 v[54:57], v[174:181], v[230:237], v[54:57], v160, v160 op_sel_hi:[0,0,0]
	s_setprio 0
	s_barrier
	s_mov_b32 m0, s64
	v_lshl_add_u64 v[140:141], v[140:141], 0, s[12:13]
	ds_read_b128 v[238:241], v164
	ds_read_b128 v[242:245], v164 offset:1024
	ds_read_b128 v[246:249], v164 offset:2048
	ds_read_b128 v[250:253], v164 offset:3072
	global_load_lds_dwordx4 v[140:141], off
	v_lshl_add_u64 v[140:141], v[142:143], 0, s[12:13]
	s_mov_b32 m0, s62
	s_nop 0
	global_load_lds_dwordx4 v[140:141], off
	s_barrier
	s_waitcnt lgkmcnt(0)
	s_setprio 1
	s_waitcnt lgkmcnt(0)
	v_mfma_scale_f32_16x16x128_f8f6f4 v[130:133], v[238:245], v[190:197], v[130:133], v160, v160 op_sel_hi:[0,0,0]
	v_mfma_scale_f32_16x16x128_f8f6f4 v[126:129], v[246:253], v[190:197], v[126:129], v160, v160 op_sel_hi:[0,0,0]
	v_mfma_scale_f32_16x16x128_f8f6f4 v[114:117], v[238:245], v[214:221], v[114:117], v160, v160 op_sel_hi:[0,0,0]
	v_mfma_scale_f32_16x16x128_f8f6f4 v[110:113], v[246:253], v[214:221], v[110:113], v160, v160 op_sel_hi:[0,0,0]
	v_mfma_scale_f32_16x16x128_f8f6f4 v[98:101], v[238:245], v[222:229], v[98:101], v160, v160 op_sel_hi:[0,0,0]
	v_mfma_scale_f32_16x16x128_f8f6f4 v[94:97], v[246:253], v[222:229], v[94:97], v160, v160 op_sel_hi:[0,0,0]
	v_mfma_scale_f32_16x16x128_f8f6f4 v[66:69], v[238:245], v[230:237], v[66:69], v160, v160 op_sel_hi:[0,0,0]
	v_mfma_scale_f32_16x16x128_f8f6f4 v[62:65], v[246:253], v[230:237], v[62:65], v160, v160 op_sel_hi:[0,0,0]
	s_setprio 0
	s_mov_b32 m0, s51
	v_lshl_add_u64 v[140:141], v[144:145], 0, s[12:13]
	s_barrier
	ds_read_b128 v[190:193], v159 offset:49152
	ds_read_b128 v[194:197], v159 offset:50176
	ds_read_b128 v[214:217], v159 offset:51200
	ds_read_b128 v[218:221], v159 offset:52224
	ds_read_b128 v[222:225], v159 offset:53248
	ds_read_b128 v[226:229], v159 offset:54272
	ds_read_b128 v[230:233], v159 offset:55296
	ds_read_b128 v[234:237], v159 offset:56320
	global_load_lds_dwordx4 v[140:141], off
	v_lshl_add_u64 v[140:141], v[154:155], 0, s[12:13]
	s_mov_b32 m0, s52
	s_nop 0
	global_load_lds_dwordx4 v[140:141], off
	s_barrier
	s_waitcnt lgkmcnt(0)
	s_setprio 1
	s_waitcnt lgkmcnt(0)
	v_mfma_scale_f32_16x16x128_f8f6f4 v[74:77], v[166:173], v[190:197], v[74:77], v160, v160 op_sel_hi:[0,0,0]
	v_mfma_scale_f32_16x16x128_f8f6f4 v[70:73], v[174:181], v[190:197], v[70:73], v160, v160 op_sel_hi:[0,0,0]
	v_mfma_scale_f32_16x16x128_f8f6f4 v[42:45], v[166:173], v[214:221], v[42:45], v160, v160 op_sel_hi:[0,0,0]
	v_mfma_scale_f32_16x16x128_f8f6f4 v[38:41], v[174:181], v[214:221], v[38:41], v160, v160 op_sel_hi:[0,0,0]
	v_mfma_scale_f32_16x16x128_f8f6f4 v[26:29], v[166:173], v[222:229], v[26:29], v160, v160 op_sel_hi:[0,0,0]
	v_mfma_scale_f32_16x16x128_f8f6f4 v[22:25], v[174:181], v[222:229], v[22:25], v160, v160 op_sel_hi:[0,0,0]
	v_mfma_scale_f32_16x16x128_f8f6f4 v[10:13], v[166:173], v[230:237], v[10:13], v160, v160 op_sel_hi:[0,0,0]
	v_mfma_scale_f32_16x16x128_f8f6f4 v[6:9], v[174:181], v[230:237], v[6:9], v160, v160 op_sel_hi:[0,0,0]
	s_setprio 0
	s_barrier
	s_add_u32 s4, s4, 0x10080
	s_addc_u32 s5, s5, 0
	s_mov_b32 m0, s45
	v_lshl_add_u64 v[140:141], s[4:5], 0, v[148:149]
	global_load_lds_dwordx4 v[140:141], off
	v_lshl_add_u64 v[140:141], s[4:5], 0, v[152:153]
	s_mov_b32 m0, s44
	s_nop 0
	global_load_lds_dwordx4 v[140:141], off
	s_waitcnt vmcnt(6)
	s_barrier
	s_setprio 1
	v_mfma_scale_f32_16x16x128_f8f6f4 v[82:85], v[238:245], v[190:197], v[82:85], v160, v160 op_sel_hi:[0,0,0]
	v_mfma_scale_f32_16x16x128_f8f6f4 v[78:81], v[246:253], v[190:197], v[78:81], v160, v160 op_sel_hi:[0,0,0]
	v_mfma_scale_f32_16x16x128_f8f6f4 v[50:53], v[238:245], v[214:221], v[50:53], v160, v160 op_sel_hi:[0,0,0]
	v_mfma_scale_f32_16x16x128_f8f6f4 v[46:49], v[246:253], v[214:221], v[46:49], v160, v160 op_sel_hi:[0,0,0]
	v_mfma_scale_f32_16x16x128_f8f6f4 v[34:37], v[238:245], v[222:229], v[34:37], v160, v160 op_sel_hi:[0,0,0]
	v_mfma_scale_f32_16x16x128_f8f6f4 v[30:33], v[246:253], v[222:229], v[30:33], v160, v160 op_sel_hi:[0,0,0]
	v_mfma_scale_f32_16x16x128_f8f6f4 v[18:21], v[238:245], v[230:237], v[18:21], v160, v160 op_sel_hi:[0,0,0]
	v_mfma_scale_f32_16x16x128_f8f6f4 v[14:17], v[246:253], v[230:237], v[14:17], v160, v160 op_sel_hi:[0,0,0]
	s_setprio 0
	s_lshl_b32 s4, s59, 7
	s_ashr_i32 s5, s4, 31
	v_lshl_add_u32 v140, s38, 8, v156
	v_bfe_u32 v234, v204, 4, 1
	v_mul_u32_u24_e32 v235, 0x3ff8, v234
	v_add_u32_e32 v232, v134, v235
	v_mov_b32_e32 v233, v135
	s_barrier
	v_mov_b32_e32 v234, v140
	v_ashrrev_i32_e32 v235, 31, v234
	v_lshlrev_b64 v[234:235], 10, v[234:235]
	v_pk_mul_f32 v[122:123], v[122:123], s[16:17] op_sel_hi:[1,0]
	v_pk_mul_f32 v[124:125], v[124:125], s[16:17] op_sel_hi:[1,0]
	v_pk_mul_f32 v[118:119], v[118:119], s[16:17] op_sel_hi:[1,0]
	v_pk_mul_f32 v[120:121], v[120:121], s[16:17] op_sel_hi:[1,0]
	v_pk_mul_f32 v[106:107], v[106:107], s[16:17] op_sel_hi:[1,0]
	v_pk_mul_f32 v[108:109], v[108:109], s[16:17] op_sel_hi:[1,0]
	v_pk_mul_f32 v[102:103], v[102:103], s[16:17] op_sel_hi:[1,0]
	v_pk_mul_f32 v[104:105], v[104:105], s[16:17] op_sel_hi:[1,0]
	v_med3_f32 v122, v122, s57, v162
	v_med3_f32 v123, v123, s57, v162
	v_med3_f32 v124, v124, s57, v162
	v_med3_f32 v125, v125, s57, v162
	v_med3_f32 v118, v118, s57, v162
	v_med3_f32 v119, v119, s57, v162
	v_med3_f32 v120, v120, s57, v162
	v_med3_f32 v121, v121, s57, v162
	v_med3_f32 v106, v106, s57, v162
	v_med3_f32 v107, v107, s57, v162
	v_med3_f32 v108, v108, s57, v162
	v_med3_f32 v109, v109, s57, v162
	v_med3_f32 v102, v102, s57, v162
	v_med3_f32 v103, v103, s57, v162
	v_med3_f32 v104, v104, s57, v162
	v_med3_f32 v105, v105, s57, v162
	v_cvt_pk_fp8_f32 v240, v122, v123
	v_cvt_pk_fp8_f32 v241, v118, v119
	v_cvt_pk_fp8_f32 v242, v106, v107
	v_cvt_pk_fp8_f32 v243, v102, v103
	v_lshl_add_u64 v[236:237], s[10:11], 0, v[234:235]
	v_cvt_pk_fp8_f32 v240, v124, v125 op_sel:[0,0,1]
	v_cvt_pk_fp8_f32 v241, v120, v121 op_sel:[0,0,1]
	v_cvt_pk_fp8_f32 v242, v108, v109 op_sel:[0,0,1]
	v_cvt_pk_fp8_f32 v243, v104, v105 op_sel:[0,0,1]
	v_lshl_add_u64 v[236:237], v[236:237], 0, s[4:5]
	v_lshl_add_u64 v[236:237], v[236:237], 0, v[232:233]
	s_nop 1
	v_permlane16_swap_b32_e32 v240, v242
	v_permlane16_swap_b32_e32 v241, v243
	s_nop 0
	global_store_dwordx4 v[236:237], v[240:243], off
	v_pk_mul_f32 v[130:131], v[130:131], s[18:19] op_sel_hi:[1,0]
	v_pk_mul_f32 v[132:133], v[132:133], s[18:19] op_sel_hi:[1,0]
	v_pk_mul_f32 v[126:127], v[126:127], s[18:19] op_sel_hi:[1,0]
	v_pk_mul_f32 v[128:129], v[128:129], s[18:19] op_sel_hi:[1,0]
	v_pk_mul_f32 v[114:115], v[114:115], s[18:19] op_sel_hi:[1,0]
	v_pk_mul_f32 v[116:117], v[116:117], s[18:19] op_sel_hi:[1,0]
	v_pk_mul_f32 v[110:111], v[110:111], s[18:19] op_sel_hi:[1,0]
	v_pk_mul_f32 v[112:113], v[112:113], s[18:19] op_sel_hi:[1,0]
	v_med3_f32 v130, v130, s57, v162
	v_med3_f32 v131, v131, s57, v162
	v_med3_f32 v132, v132, s57, v162
	v_med3_f32 v133, v133, s57, v162
	v_med3_f32 v126, v126, s57, v162
	v_med3_f32 v127, v127, s57, v162
	v_med3_f32 v128, v128, s57, v162
	v_med3_f32 v129, v129, s57, v162
	v_med3_f32 v114, v114, s57, v162
	v_med3_f32 v115, v115, s57, v162
	v_med3_f32 v116, v116, s57, v162
	v_med3_f32 v117, v117, s57, v162
	v_med3_f32 v110, v110, s57, v162
	v_med3_f32 v111, v111, s57, v162
	v_med3_f32 v112, v112, s57, v162
	v_med3_f32 v113, v113, s57, v162
	v_cvt_pk_fp8_f32 v244, v130, v131
	v_cvt_pk_fp8_f32 v245, v126, v127
	v_cvt_pk_fp8_f32 v246, v114, v115
	v_cvt_pk_fp8_f32 v247, v110, v111
	v_lshl_add_u64 v[238:239], s[8:9], 0, v[234:235]
	v_cvt_pk_fp8_f32 v244, v132, v133 op_sel:[0,0,1]
	v_cvt_pk_fp8_f32 v245, v128, v129 op_sel:[0,0,1]
	v_cvt_pk_fp8_f32 v246, v116, v117 op_sel:[0,0,1]
	v_cvt_pk_fp8_f32 v247, v112, v113 op_sel:[0,0,1]
	v_lshl_add_u64 v[238:239], v[238:239], 0, s[4:5]
	v_lshl_add_u64 v[238:239], v[238:239], 0, v[232:233]
	s_nop 1
	v_permlane16_swap_b32_e32 v244, v246
	v_permlane16_swap_b32_e32 v245, v247
	s_nop 0
	global_store_dwordx4 v[238:239], v[244:247], off
	v_or_b32_e32 v234, 32, v140
	v_ashrrev_i32_e32 v235, 31, v234
	v_lshlrev_b64 v[234:235], 10, v[234:235]
	v_pk_mul_f32 v[90:91], v[90:91], s[16:17] op_sel_hi:[1,0]
	v_pk_mul_f32 v[92:93], v[92:93], s[16:17] op_sel_hi:[1,0]
	v_pk_mul_f32 v[86:87], v[86:87], s[16:17] op_sel_hi:[1,0]
	v_pk_mul_f32 v[88:89], v[88:89], s[16:17] op_sel_hi:[1,0]
	v_pk_mul_f32 v[58:59], v[58:59], s[16:17] op_sel_hi:[1,0]
	v_pk_mul_f32 v[60:61], v[60:61], s[16:17] op_sel_hi:[1,0]
	v_pk_mul_f32 v[54:55], v[54:55], s[16:17] op_sel_hi:[1,0]
	v_pk_mul_f32 v[56:57], v[56:57], s[16:17] op_sel_hi:[1,0]
	v_med3_f32 v90, v90, s57, v162
	v_med3_f32 v91, v91, s57, v162
	v_med3_f32 v92, v92, s57, v162
	v_med3_f32 v93, v93, s57, v162
	v_med3_f32 v86, v86, s57, v162
	v_med3_f32 v87, v87, s57, v162
	v_med3_f32 v88, v88, s57, v162
	v_med3_f32 v89, v89, s57, v162
	v_med3_f32 v58, v58, s57, v162
	v_med3_f32 v59, v59, s57, v162
	v_med3_f32 v60, v60, s57, v162
	v_med3_f32 v61, v61, s57, v162
	v_med3_f32 v54, v54, s57, v162
	v_med3_f32 v55, v55, s57, v162
	v_med3_f32 v56, v56, s57, v162
	v_med3_f32 v57, v57, s57, v162
	v_cvt_pk_fp8_f32 v240, v90, v91
	v_cvt_pk_fp8_f32 v241, v86, v87
	v_cvt_pk_fp8_f32 v242, v58, v59
	v_cvt_pk_fp8_f32 v243, v54, v55
	v_lshl_add_u64 v[236:237], s[10:11], 0, v[234:235]
	v_cvt_pk_fp8_f32 v240, v92, v93 op_sel:[0,0,1]
	v_cvt_pk_fp8_f32 v241, v88, v89 op_sel:[0,0,1]
	v_cvt_pk_fp8_f32 v242, v60, v61 op_sel:[0,0,1]
	v_cvt_pk_fp8_f32 v243, v56, v57 op_sel:[0,0,1]
	v_lshl_add_u64 v[236:237], v[236:237], 0, s[4:5]
	v_lshl_add_u64 v[236:237], v[236:237], 0, v[232:233]
	s_nop 1
	v_permlane16_swap_b32_e32 v240, v242
	v_permlane16_swap_b32_e32 v241, v243
	s_nop 0
	global_store_dwordx4 v[236:237], v[240:243], off
	v_pk_mul_f32 v[98:99], v[98:99], s[18:19] op_sel_hi:[1,0]
	v_pk_mul_f32 v[100:101], v[100:101], s[18:19] op_sel_hi:[1,0]
	v_pk_mul_f32 v[94:95], v[94:95], s[18:19] op_sel_hi:[1,0]
	v_pk_mul_f32 v[96:97], v[96:97], s[18:19] op_sel_hi:[1,0]
	v_pk_mul_f32 v[66:67], v[66:67], s[18:19] op_sel_hi:[1,0]
	v_pk_mul_f32 v[68:69], v[68:69], s[18:19] op_sel_hi:[1,0]
	v_pk_mul_f32 v[62:63], v[62:63], s[18:19] op_sel_hi:[1,0]
	v_pk_mul_f32 v[64:65], v[64:65], s[18:19] op_sel_hi:[1,0]
	v_med3_f32 v98, v98, s57, v162
	v_med3_f32 v99, v99, s57, v162
	v_med3_f32 v100, v100, s57, v162
	v_med3_f32 v101, v101, s57, v162
	v_med3_f32 v94, v94, s57, v162
	v_med3_f32 v95, v95, s57, v162
	v_med3_f32 v96, v96, s57, v162
	v_med3_f32 v97, v97, s57, v162
	v_med3_f32 v66, v66, s57, v162
	v_med3_f32 v67, v67, s57, v162
	v_med3_f32 v68, v68, s57, v162
	v_med3_f32 v69, v69, s57, v162
	v_med3_f32 v62, v62, s57, v162
	v_med3_f32 v63, v63, s57, v162
	v_med3_f32 v64, v64, s57, v162
	v_med3_f32 v65, v65, s57, v162
	v_cvt_pk_fp8_f32 v244, v98, v99
	v_cvt_pk_fp8_f32 v245, v94, v95
	v_cvt_pk_fp8_f32 v246, v66, v67
	v_cvt_pk_fp8_f32 v247, v62, v63
	v_lshl_add_u64 v[238:239], s[8:9], 0, v[234:235]
	v_cvt_pk_fp8_f32 v244, v100, v101 op_sel:[0,0,1]
	v_cvt_pk_fp8_f32 v245, v96, v97 op_sel:[0,0,1]
	v_cvt_pk_fp8_f32 v246, v68, v69 op_sel:[0,0,1]
	v_cvt_pk_fp8_f32 v247, v64, v65 op_sel:[0,0,1]
	v_lshl_add_u64 v[238:239], v[238:239], 0, s[4:5]
	v_lshl_add_u64 v[238:239], v[238:239], 0, v[232:233]
	s_nop 1
	v_permlane16_swap_b32_e32 v244, v246
	v_permlane16_swap_b32_e32 v245, v247
	s_nop 0
	global_store_dwordx4 v[238:239], v[244:247], off
	v_or_b32_e32 v234, 128, v140
	v_ashrrev_i32_e32 v235, 31, v234
	v_lshlrev_b64 v[234:235], 10, v[234:235]
	v_pk_mul_f32 v[74:75], v[74:75], s[16:17] op_sel_hi:[1,0]
	v_pk_mul_f32 v[76:77], v[76:77], s[16:17] op_sel_hi:[1,0]
	v_pk_mul_f32 v[70:71], v[70:71], s[16:17] op_sel_hi:[1,0]
	v_pk_mul_f32 v[72:73], v[72:73], s[16:17] op_sel_hi:[1,0]
	v_pk_mul_f32 v[42:43], v[42:43], s[16:17] op_sel_hi:[1,0]
	v_pk_mul_f32 v[44:45], v[44:45], s[16:17] op_sel_hi:[1,0]
	v_pk_mul_f32 v[38:39], v[38:39], s[16:17] op_sel_hi:[1,0]
	v_pk_mul_f32 v[40:41], v[40:41], s[16:17] op_sel_hi:[1,0]
	v_med3_f32 v74, v74, s57, v162
	v_med3_f32 v75, v75, s57, v162
	v_med3_f32 v76, v76, s57, v162
	v_med3_f32 v77, v77, s57, v162
	v_med3_f32 v70, v70, s57, v162
	v_med3_f32 v71, v71, s57, v162
	v_med3_f32 v72, v72, s57, v162
	v_med3_f32 v73, v73, s57, v162
	v_med3_f32 v42, v42, s57, v162
	v_med3_f32 v43, v43, s57, v162
	v_med3_f32 v44, v44, s57, v162
	v_med3_f32 v45, v45, s57, v162
	v_med3_f32 v38, v38, s57, v162
	v_med3_f32 v39, v39, s57, v162
	v_med3_f32 v40, v40, s57, v162
	v_med3_f32 v41, v41, s57, v162
	v_cvt_pk_fp8_f32 v240, v74, v75
	v_cvt_pk_fp8_f32 v241, v70, v71
	v_cvt_pk_fp8_f32 v242, v42, v43
	v_cvt_pk_fp8_f32 v243, v38, v39
	v_lshl_add_u64 v[236:237], s[10:11], 0, v[234:235]
	v_cvt_pk_fp8_f32 v240, v76, v77 op_sel:[0,0,1]
	v_cvt_pk_fp8_f32 v241, v72, v73 op_sel:[0,0,1]
	v_cvt_pk_fp8_f32 v242, v44, v45 op_sel:[0,0,1]
	v_cvt_pk_fp8_f32 v243, v40, v41 op_sel:[0,0,1]
	v_lshl_add_u64 v[236:237], v[236:237], 0, s[4:5]
	v_lshl_add_u64 v[236:237], v[236:237], 0, v[232:233]
	s_nop 1
	v_permlane16_swap_b32_e32 v240, v242
	v_permlane16_swap_b32_e32 v241, v243
	s_nop 0
	global_store_dwordx4 v[236:237], v[240:243], off
	v_pk_mul_f32 v[82:83], v[82:83], s[18:19] op_sel_hi:[1,0]
	v_pk_mul_f32 v[84:85], v[84:85], s[18:19] op_sel_hi:[1,0]
	v_pk_mul_f32 v[78:79], v[78:79], s[18:19] op_sel_hi:[1,0]
	v_pk_mul_f32 v[80:81], v[80:81], s[18:19] op_sel_hi:[1,0]
	v_pk_mul_f32 v[50:51], v[50:51], s[18:19] op_sel_hi:[1,0]
	v_pk_mul_f32 v[52:53], v[52:53], s[18:19] op_sel_hi:[1,0]
	v_pk_mul_f32 v[46:47], v[46:47], s[18:19] op_sel_hi:[1,0]
	v_pk_mul_f32 v[48:49], v[48:49], s[18:19] op_sel_hi:[1,0]
	v_med3_f32 v82, v82, s57, v162
	v_med3_f32 v83, v83, s57, v162
	v_med3_f32 v84, v84, s57, v162
	v_med3_f32 v85, v85, s57, v162
	v_med3_f32 v78, v78, s57, v162
	v_med3_f32 v79, v79, s57, v162
	v_med3_f32 v80, v80, s57, v162
	v_med3_f32 v81, v81, s57, v162
	v_med3_f32 v50, v50, s57, v162
	v_med3_f32 v51, v51, s57, v162
	v_med3_f32 v52, v52, s57, v162
	v_med3_f32 v53, v53, s57, v162
	v_med3_f32 v46, v46, s57, v162
	v_med3_f32 v47, v47, s57, v162
	v_med3_f32 v48, v48, s57, v162
	v_med3_f32 v49, v49, s57, v162
	v_cvt_pk_fp8_f32 v244, v82, v83
	v_cvt_pk_fp8_f32 v245, v78, v79
	v_cvt_pk_fp8_f32 v246, v50, v51
	v_cvt_pk_fp8_f32 v247, v46, v47
	v_lshl_add_u64 v[238:239], s[8:9], 0, v[234:235]
	v_cvt_pk_fp8_f32 v244, v84, v85 op_sel:[0,0,1]
	v_cvt_pk_fp8_f32 v245, v80, v81 op_sel:[0,0,1]
	v_cvt_pk_fp8_f32 v246, v52, v53 op_sel:[0,0,1]
	v_cvt_pk_fp8_f32 v247, v48, v49 op_sel:[0,0,1]
	v_lshl_add_u64 v[238:239], v[238:239], 0, s[4:5]
	v_lshl_add_u64 v[238:239], v[238:239], 0, v[232:233]
	s_nop 1
	v_permlane16_swap_b32_e32 v244, v246
	v_permlane16_swap_b32_e32 v245, v247
	s_nop 0
	global_store_dwordx4 v[238:239], v[244:247], off
	v_or_b32_e32 v234, 160, v140
	v_ashrrev_i32_e32 v235, 31, v234
	v_lshlrev_b64 v[234:235], 10, v[234:235]
	v_pk_mul_f32 v[26:27], v[26:27], s[16:17] op_sel_hi:[1,0]
	v_pk_mul_f32 v[28:29], v[28:29], s[16:17] op_sel_hi:[1,0]
	v_pk_mul_f32 v[22:23], v[22:23], s[16:17] op_sel_hi:[1,0]
	v_pk_mul_f32 v[24:25], v[24:25], s[16:17] op_sel_hi:[1,0]
	v_pk_mul_f32 v[10:11], v[10:11], s[16:17] op_sel_hi:[1,0]
	v_pk_mul_f32 v[12:13], v[12:13], s[16:17] op_sel_hi:[1,0]
	v_pk_mul_f32 v[6:7], v[6:7], s[16:17] op_sel_hi:[1,0]
	v_pk_mul_f32 v[8:9], v[8:9], s[16:17] op_sel_hi:[1,0]
	v_med3_f32 v26, v26, s57, v162
	v_med3_f32 v27, v27, s57, v162
	v_med3_f32 v28, v28, s57, v162
	v_med3_f32 v29, v29, s57, v162
	v_med3_f32 v22, v22, s57, v162
	v_med3_f32 v23, v23, s57, v162
	v_med3_f32 v24, v24, s57, v162
	v_med3_f32 v25, v25, s57, v162
	v_med3_f32 v10, v10, s57, v162
	v_med3_f32 v11, v11, s57, v162
	v_med3_f32 v12, v12, s57, v162
	v_med3_f32 v13, v13, s57, v162
	v_med3_f32 v6, v6, s57, v162
	v_med3_f32 v7, v7, s57, v162
	v_med3_f32 v8, v8, s57, v162
	v_med3_f32 v9, v9, s57, v162
	v_cvt_pk_fp8_f32 v240, v26, v27
	v_cvt_pk_fp8_f32 v241, v22, v23
	v_cvt_pk_fp8_f32 v242, v10, v11
	v_cvt_pk_fp8_f32 v243, v6, v7
	v_lshl_add_u64 v[236:237], s[10:11], 0, v[234:235]
	v_cvt_pk_fp8_f32 v240, v28, v29 op_sel:[0,0,1]
	v_cvt_pk_fp8_f32 v241, v24, v25 op_sel:[0,0,1]
	v_cvt_pk_fp8_f32 v242, v12, v13 op_sel:[0,0,1]
	v_cvt_pk_fp8_f32 v243, v8, v9 op_sel:[0,0,1]
	v_lshl_add_u64 v[236:237], v[236:237], 0, s[4:5]
	v_lshl_add_u64 v[236:237], v[236:237], 0, v[232:233]
	s_nop 1
	v_permlane16_swap_b32_e32 v240, v242
	v_permlane16_swap_b32_e32 v241, v243
	s_nop 0
	global_store_dwordx4 v[236:237], v[240:243], off
	v_pk_mul_f32 v[34:35], v[34:35], s[18:19] op_sel_hi:[1,0]
	v_pk_mul_f32 v[36:37], v[36:37], s[18:19] op_sel_hi:[1,0]
	v_pk_mul_f32 v[30:31], v[30:31], s[18:19] op_sel_hi:[1,0]
	v_pk_mul_f32 v[32:33], v[32:33], s[18:19] op_sel_hi:[1,0]
	v_pk_mul_f32 v[18:19], v[18:19], s[18:19] op_sel_hi:[1,0]
	v_pk_mul_f32 v[20:21], v[20:21], s[18:19] op_sel_hi:[1,0]
	v_pk_mul_f32 v[14:15], v[14:15], s[18:19] op_sel_hi:[1,0]
	v_pk_mul_f32 v[16:17], v[16:17], s[18:19] op_sel_hi:[1,0]
	v_med3_f32 v34, v34, s57, v162
	v_med3_f32 v35, v35, s57, v162
	v_med3_f32 v36, v36, s57, v162
	v_med3_f32 v37, v37, s57, v162
	v_med3_f32 v30, v30, s57, v162
	v_med3_f32 v31, v31, s57, v162
	v_med3_f32 v32, v32, s57, v162
	v_med3_f32 v33, v33, s57, v162
	v_med3_f32 v18, v18, s57, v162
	v_med3_f32 v19, v19, s57, v162
	v_med3_f32 v20, v20, s57, v162
	v_med3_f32 v21, v21, s57, v162
	v_med3_f32 v14, v14, s57, v162
	v_med3_f32 v15, v15, s57, v162
	v_med3_f32 v16, v16, s57, v162
	v_med3_f32 v17, v17, s57, v162
	v_cvt_pk_fp8_f32 v244, v34, v35
	v_cvt_pk_fp8_f32 v245, v30, v31
	v_cvt_pk_fp8_f32 v246, v18, v19
	v_cvt_pk_fp8_f32 v247, v14, v15
	v_lshl_add_u64 v[238:239], s[8:9], 0, v[234:235]
	v_cvt_pk_fp8_f32 v244, v36, v37 op_sel:[0,0,1]
	v_cvt_pk_fp8_f32 v245, v32, v33 op_sel:[0,0,1]
	v_cvt_pk_fp8_f32 v246, v20, v21 op_sel:[0,0,1]
	v_cvt_pk_fp8_f32 v247, v16, v17 op_sel:[0,0,1]
	v_lshl_add_u64 v[238:239], v[238:239], 0, s[4:5]
	v_lshl_add_u64 v[238:239], v[238:239], 0, v[232:233]
	s_nop 1
	v_permlane16_swap_b32_e32 v244, v246
	v_permlane16_swap_b32_e32 v245, v247
	s_nop 0
	global_store_dwordx4 v[238:239], v[244:247], off
	v_readlane_b32 s40, v254, 42
	s_add_i32 s54, s54, s40
	s_andn2_b64 vcc, exec, s[0:1]
	s_mov_b32 s59, s28
	s_mov_b32 s38, s30
	s_mov_b64 s[44:45], s[36:37]
	s_mov_b64 s[42:43], s[34:35]
	v_readlane_b32 s41, v254, 43
	s_cbranch_vccz .LBB0_954
